# plus post-projection Q/K row loop: next trip rows prefetched one trip ahead
# baseline (speedup 1.0000x reference)
.LBB0_771:
	s_or_b64 exec, exec, s[6:7]
	v_ashrrev_i32_e32 v3, 31, v2
	v_lshl_add_u64 v[2:3], v[2:3], 3, s[0:1]
	global_load_dwordx2 v[2:3], v[2:3], off
	v_and_b32_e32 v19, 3, v18
	s_lshl_b32 s70, s73, 6
	v_lshlrev_b32_e32 v0, 6, v19
	s_mov_b32 s6, 35
	v_lshl_or_b32 v54, s8, 6, v18
	v_ashrrev_i32_e32 v55, 31, v54
	s_waitcnt vmcnt(0)
	v_lshl_add_u64 v[2:3], s[70:71], 2, v[2:3]
	v_lshl_add_u64 v[14:15], v[2:3], 0, v[0:1]
	global_load_dwordx4 v[2:5], v[14:15], off offset:48
	global_load_dwordx4 v[6:9], v[14:15], off offset:32
	global_load_dwordx4 v[10:13], v[14:15], off offset:16
	s_nop 0
	global_load_dwordx4 v[14:17], v[14:15], off
	s_barrier
	s_ashr_i32 s7, s6, 31
	s_lshl_b64 s[6:7], s[6:7], 3
	s_add_u32 s6, s0, s6
	s_addc_u32 s7, s1, s7
	s_load_dwordx2 s[6:7], s[6:7], 0x0
	v_lshl_add_u32 v0, v54, 4, 0
	s_waitcnt lgkmcnt(0)
	v_lshl_add_u64 v[20:21], v[54:55], 4, s[6:7]
	s_mov_b32 s6, 0x600000
	v_add_co_u32_e32 v20, vcc, s6, v20
	v_readlane_b32 s6, v254, 12
	s_nop 0
	v_addc_co_u32_e32 v21, vcc, 0, v21, vcc
	global_load_dwordx4 v[20:23], v[20:21], off
	s_waitcnt vmcnt(0)
	ds_write_b128 v0, v[20:23]
	v_ashrrev_i32_e32 v0, 5, v54
	v_and_b32_e32 v0, -2, v0
	v_add_u32_e32 v26, s6, v0
	s_mov_b32 s6, 0x8800
	v_cmp_gt_i32_e32 vcc, s6, v26
	s_waitcnt lgkmcnt(0)
	s_barrier
	s_and_saveexec_b64 s[22:23], vcc
	s_cbranch_execz .LBB0_806
	v_cmp_gt_u32_e64 s[6:7], 8, v52
	v_mov_b32_e32 v0, 0x380
	v_mov_b32_e32 v20, 0x300
	v_cndmask_b32_e64 v0, v0, v20, s[6:7]
	v_lshlrev_b32_e32 v22, 6, v52
	v_and_b32_e32 v18, 1, v18
	v_ashrrev_i32_e32 v27, 31, v26
	v_cmp_eq_u32_e64 s[10:11], 0, v18
	v_lshlrev_b64 v[20:21], 12, v[26:27]
	v_lshlrev_b32_e32 v18, 5, v19
	v_add_lshl_u32 v0, v0, v22, 1
	v_or3_b32 v20, v20, v18, v0
	v_lshlrev_b32_e32 v53, 4, v19
	v_cmp_gt_u32_e64 s[8:9], 2, v19
	v_cmp_lt_u32_e32 vcc, 13, v52
	v_lshl_add_u64 v[18:19], s[20:21], 0, v[20:21]
	s_mov_b64 s[12:13], 0x27801010
	v_cndmask_b32_e64 v55, 0, 8, vcc
	v_bfe_u32 v56, v54, 2, 1
	v_lshl_add_u64 v[28:29], v[18:19], 0, s[12:13]
	s_mov_b64 s[24:25], 0
	v_add_co_u32_e32 v208, vcc, 0xfffff000, v28
	s_nop 1
	v_addc_co_u32_e32 v209, vcc, -1, v29, vcc
	global_load_dwordx4 v[188:191], v[208:209], off offset:-16
	global_load_dwordx4 v[192:195], v[28:29], off offset:-4096
	global_load_dwordx4 v[196:199], v[28:29], off
	global_load_dwordx4 v[200:203], v[28:29], off offset:-16
	s_waitcnt vmcnt(0)
	s_branch .LBB0_774

.LBB0_774:
	s_waitcnt vmcnt(4)
	v_mov_b32_e32 v36, v188
	v_mov_b32_e32 v37, v189
	v_mov_b32_e32 v38, v190
	v_mov_b32_e32 v39, v191
	v_mov_b32_e32 v44, v192
	v_mov_b32_e32 v45, v193
	v_mov_b32_e32 v46, v194
	v_mov_b32_e32 v47, v195
	v_mov_b32_e32 v18, v196
	v_mov_b32_e32 v19, v197
	v_mov_b32_e32 v20, v198
	v_mov_b32_e32 v21, v199
	v_mov_b32_e32 v22, v200
	v_mov_b32_e32 v23, v201
	v_mov_b32_e32 v24, v202
	v_mov_b32_e32 v25, v203
	v_readlane_b32 s12, v255, 35
	v_readlane_b32 s13, v255, 36
	s_nop 1
	v_lshl_add_u64 v[206:207], v[28:29], 0, s[12:13]
	v_add_co_u32_e32 v208, vcc, 0xfffff000, v206
	s_nop 1
	v_addc_co_u32_e32 v209, vcc, -1, v207, vcc
	global_load_dwordx4 v[188:191], v[208:209], off offset:-16
	global_load_dwordx4 v[192:195], v[206:207], off offset:-4096
	global_load_dwordx4 v[196:199], v[206:207], off
	global_load_dwordx4 v[200:203], v[206:207], off offset:-16
	s_nop 0
	v_lshlrev_b32_e32 v32, 16, v36
	v_and_b32_e32 v33, 0xffff0000, v36
	v_lshlrev_b32_e32 v34, 16, v37
	v_and_b32_e32 v35, 0xffff0000, v37
	v_lshlrev_b32_e32 v36, 16, v38
	v_and_b32_e32 v37, 0xffff0000, v38
	v_lshlrev_b32_e32 v38, 16, v39
	v_and_b32_e32 v39, 0xffff0000, v39
	s_nop 0
	v_lshlrev_b32_e32 v40, 16, v44
	v_and_b32_e32 v41, 0xffff0000, v44
	v_lshlrev_b32_e32 v42, 16, v45
	v_and_b32_e32 v43, 0xffff0000, v45
	v_lshlrev_b32_e32 v44, 16, v46
	v_and_b32_e32 v45, 0xffff0000, v46
	v_and_b32_e32 v30, 0xffff0000, v47
	v_lshlrev_b32_e32 v31, 16, v47
	s_and_saveexec_b64 s[12:13], s[6:7]
	s_cbranch_execz .LBB0_776
	v_pk_mul_f32 v[46:47], v[32:33], v[32:33]
	v_pk_mul_f32 v[48:49], v[34:35], v[34:35]
	v_add_f32_e32 v0, v46, v47
	v_add_f32_e32 v0, v48, v0
	v_pk_mul_f32 v[50:51], v[36:37], v[36:37]
	v_add_f32_e32 v0, v49, v0
	v_add_f32_e32 v0, v50, v0
	v_pk_mul_f32 v[58:59], v[38:39], v[38:39]
	v_add_f32_e32 v0, v51, v0
	v_add_f32_e32 v0, v58, v0
	v_pk_mul_f32 v[60:61], v[40:41], v[40:41]
	v_add_f32_e32 v0, v59, v0
	v_add_f32_e32 v0, v60, v0
	v_pk_mul_f32 v[62:63], v[42:43], v[42:43]
	v_add_f32_e32 v0, v61, v0
	v_add_f32_e32 v0, v62, v0
	v_pk_mul_f32 v[64:65], v[44:45], v[44:45]
	v_add_f32_e32 v0, v63, v0
	v_add_f32_e32 v0, v64, v0
	v_pk_mul_f32 v[66:67], v[30:31], v[30:31]
	v_add_f32_e32 v0, v65, v0
	v_add_f32_e32 v0, v67, v0
	v_add_f32_e32 v0, v66, v0
	v_mov_b32_e32 v46, 0x358637bd
	s_nop 0
	v_add_f32_dpp v0, v0, v0 quad_perm:[1,0,3,2] row_mask:0xf bank_mask:0xf bound_ctrl:1
	s_nop 1
	v_add_f32_dpp v0, v0, v0 quad_perm:[2,3,0,1] row_mask:0xf bank_mask:0xf bound_ctrl:1
	v_fmamk_f32 v0, v0, 0x3c800000, v46
	v_mul_f32_e32 v27, 0x4b800000, v0
	v_cmp_gt_f32_e32 vcc, s59, v0
	s_nop 1
	v_cndmask_b32_e32 v0, v0, v27, vcc
	v_rsq_f32_e32 v0, v0
	s_nop 0
	v_mul_f32_e32 v27, 0x45800000, v0
	v_cndmask_b32_e32 v0, v0, v27, vcc
	v_pk_mul_f32 v[30:31], v[0:1], v[30:31] op_sel_hi:[0,1]
	v_pk_mul_f32 v[32:33], v[0:1], v[32:33] op_sel_hi:[0,1]
	v_pk_mul_f32 v[34:35], v[0:1], v[34:35] op_sel_hi:[0,1]
	v_pk_mul_f32 v[36:37], v[0:1], v[36:37] op_sel_hi:[0,1]
	v_pk_mul_f32 v[38:39], v[0:1], v[38:39] op_sel_hi:[0,1]
	v_pk_mul_f32 v[40:41], v[0:1], v[40:41] op_sel_hi:[0,1]
	v_pk_mul_f32 v[42:43], v[0:1], v[42:43] op_sel_hi:[0,1]
	v_pk_mul_f32 v[44:45], v[0:1], v[44:45] op_sel_hi:[0,1]
	v_pk_mul_f32 v[46:47], v[4:5], v[30:31] op_sel:[0,1] op_sel_hi:[1,0]
	v_pk_mul_f32 v[32:33], v[14:15], v[32:33]
	v_pk_mul_f32 v[34:35], v[16:17], v[34:35]
	v_pk_mul_f32 v[36:37], v[10:11], v[36:37]
	v_pk_mul_f32 v[38:39], v[12:13], v[38:39]
	v_pk_mul_f32 v[40:41], v[6:7], v[40:41]
	v_pk_mul_f32 v[42:43], v[8:9], v[42:43]
	v_pk_mul_f32 v[44:45], v[2:3], v[44:45]
	v_mov_b32_e32 v31, v46
	v_mov_b32_e32 v30, v47

.LBB0_786:
	s_or_b64 exec, exec, s[26:27]
	v_cvt_pk_bf16_f32 v32, v32, v33
	v_cvt_pk_bf16_f32 v33, v34, v35
	v_cvt_pk_bf16_f32 v34, v36, v37
	v_cvt_pk_bf16_f32 v35, v38, v39
	v_cvt_pk_bf16_f32 v36, v40, v41
	v_cvt_pk_bf16_f32 v37, v42, v43
	v_cvt_pk_bf16_f32 v38, v44, v45
	v_cvt_pk_bf16_f32 v39, v46, v47
	global_store_dwordx4 v[50:51], v[32:35], off
	global_store_dwordx4 v[50:51], v[36:39], off offset:16
	s_nop 0
	v_and_b32_e32 v42, 0xffff0000, v21
	s_nop 0
	v_lshlrev_b32_e32 v32, 16, v22
	v_and_b32_e32 v33, 0xffff0000, v22
	v_lshlrev_b32_e32 v22, 16, v23
	v_and_b32_e32 v23, 0xffff0000, v23
	v_lshlrev_b32_e32 v34, 16, v24
	v_and_b32_e32 v35, 0xffff0000, v24
	v_lshlrev_b32_e32 v36, 16, v25
	v_and_b32_e32 v37, 0xffff0000, v25
	v_lshlrev_b32_e32 v24, 16, v18
	v_and_b32_e32 v25, 0xffff0000, v18
	v_lshlrev_b32_e32 v18, 16, v19
	v_and_b32_e32 v19, 0xffff0000, v19
	v_lshlrev_b32_e32 v38, 16, v20
	v_and_b32_e32 v39, 0xffff0000, v20
	v_lshlrev_b32_e32 v43, 16, v21
	s_and_saveexec_b64 s[26:27], s[6:7]
	s_cbranch_execz .LBB0_788
	v_pk_mul_f32 v[20:21], v[32:33], v[32:33]
	v_pk_mul_f32 v[40:41], v[22:23], v[22:23]
	v_add_f32_e32 v20, v20, v21
	v_add_f32_e32 v20, v40, v20
	v_pk_mul_f32 v[44:45], v[34:35], v[34:35]
	v_add_f32_e32 v20, v41, v20
	v_add_f32_e32 v20, v44, v20
	v_pk_mul_f32 v[46:47], v[36:37], v[36:37]
	v_add_f32_e32 v20, v45, v20
	v_add_f32_e32 v20, v46, v20
	v_pk_mul_f32 v[48:49], v[24:25], v[24:25]
	v_add_f32_e32 v20, v47, v20
	v_add_f32_e32 v20, v48, v20
	v_pk_mul_f32 v[50:51], v[18:19], v[18:19]
	v_add_f32_e32 v20, v49, v20
	v_add_f32_e32 v20, v50, v20
	v_pk_mul_f32 v[58:59], v[38:39], v[38:39]
	v_add_f32_e32 v20, v51, v20
	v_add_f32_e32 v20, v58, v20
	v_pk_mul_f32 v[60:61], v[42:43], v[42:43]
	v_add_f32_e32 v20, v59, v20
	v_add_f32_e32 v20, v61, v20
	v_add_f32_e32 v20, v60, v20
	v_mov_b32_e32 v40, 0x358637bd
	s_nop 0
	v_add_f32_dpp v20, v20, v20 quad_perm:[1,0,3,2] row_mask:0xf bank_mask:0xf bound_ctrl:1
	s_nop 1
	v_add_f32_dpp v20, v20, v20 quad_perm:[2,3,0,1] row_mask:0xf bank_mask:0xf bound_ctrl:1
	v_fmamk_f32 v20, v20, 0x3c800000, v40
	v_mul_f32_e32 v21, 0x4b800000, v20
	v_cmp_gt_f32_e64 s[18:19], s59, v20
	s_nop 1
	v_cndmask_b32_e64 v20, v20, v21, s[18:19]
	v_rsq_f32_e32 v20, v20
	s_nop 0
	v_mul_f32_e32 v21, 0x45800000, v20
	v_cndmask_b32_e64 v20, v20, v21, s[18:19]
	v_pk_mul_f32 v[32:33], v[20:21], v[32:33] op_sel_hi:[0,1]
	v_pk_mul_f32 v[22:23], v[20:21], v[22:23] op_sel_hi:[0,1]
	v_pk_mul_f32 v[34:35], v[20:21], v[34:35] op_sel_hi:[0,1]
	v_pk_mul_f32 v[36:37], v[20:21], v[36:37] op_sel_hi:[0,1]
	v_pk_mul_f32 v[24:25], v[20:21], v[24:25] op_sel_hi:[0,1]
	v_pk_mul_f32 v[18:19], v[20:21], v[18:19] op_sel_hi:[0,1]
	v_pk_mul_f32 v[38:39], v[20:21], v[38:39] op_sel_hi:[0,1]
	v_pk_mul_f32 v[20:21], v[20:21], v[42:43] op_sel_hi:[0,1]
	v_pk_mul_f32 v[20:21], v[4:5], v[20:21] op_sel:[0,1] op_sel_hi:[1,0]
	v_pk_mul_f32 v[32:33], v[14:15], v[32:33]
	v_pk_mul_f32 v[22:23], v[16:17], v[22:23]
	v_pk_mul_f32 v[34:35], v[10:11], v[34:35]
	v_pk_mul_f32 v[36:37], v[12:13], v[36:37]
	v_pk_mul_f32 v[24:25], v[6:7], v[24:25]
	v_pk_mul_f32 v[18:19], v[8:9], v[18:19]
	v_pk_mul_f32 v[38:39], v[2:3], v[38:39]
	v_mov_b32_e32 v43, v20
	v_mov_b32_e32 v42, v21
